# v_qk + micro cleanup: SALU s_not for complement tile masks (32 fewer VALU/head), 16-instr zero-init, lgkmcnt(2) at barrier A
# speedup vs baseline: 1.0254x; 1.0254x over previous
.LBB1_6:
	v_mov_b32_e32 v195, v194
	v_mov_b32_e32 v196, v194
	v_mov_b32_e32 v197, v194
	s_setprio 1
	s_and_b64 vcc, exec, s[2:3]
	s_cbranch_vccnz .LBB1_61
	s_not_b64 s[16:17], s[0:1]
	s_andn2_b64 vcc, exec, s[0:1]
	s_cbranch_vccz .LBB1_62
.LBB1_8:
	s_not_b64 s[18:19], s[6:7]
	s_andn2_b64 vcc, exec, s[6:7]
	s_cbranch_vccz .LBB1_63
.LBB1_9:
	s_not_b64 s[20:21], s[4:5]
	s_andn2_b64 vcc, exec, s[4:5]
	s_cbranch_vccnz .LBB1_11

.Ltri1_done:
	s_cmp_lg_u32 s36, 0x60000
	s_cselect_b64 s[52:53], -1, 0
	s_cmp_eq_u32 s36, 0x60000
	s_cselect_b32 s23, s27, s55
	s_cselect_b32 s22, s26, s54
	s_setprio 0
	v_readfirstlane_b32 s24, v224
	s_mov_b32 m0, s24
	v_readfirstlane_b32 s24, v225
	global_load_lds_dwordx4 v223, s[22:23]
	s_mov_b32 m0, s24
	v_readfirstlane_b32 s24, v213
	global_load_lds_dwordx4 v210, s[22:23]
	s_mov_b32 m0, s24
	v_readfirstlane_b32 s24, v215
	global_load_lds_dwordx4 v212, s[22:23]
	s_mov_b32 m0, s24
	s_nop 0
	global_load_lds_dwordx4 v214, s[22:23]
	v_mov_b32_e32 v243, 0xff800000
	s_not_b64 s[22:23], s[2:3]
	s_andn2_b64 vcc, exec, s[2:3]
	v_mov_b32_e32 v1, 0xff800000
	s_cbranch_vccz .LBB1_64
	s_and_b64 vcc, exec, s[22:23]
	s_cbranch_vccz .LBB1_65

.LBB1_32:
	s_setprio 0
	s_setprio 1
	s_not_b64 s[18:19], s[10:11]
	s_andn2_b64 vcc, exec, s[10:11]
	s_cbranch_vccz .LBB1_71
	s_not_b64 s[20:21], s[8:9]
	s_andn2_b64 vcc, exec, s[8:9]
	s_cbranch_vccz .LBB1_72
.LBB1_34:
	s_not_b64 s[22:23], s[14:15]
	s_andn2_b64 vcc, exec, s[14:15]
	s_cbranch_vccz .LBB1_73
.LBB1_35:
	s_not_b64 s[24:25], s[12:13]
	s_andn2_b64 vcc, exec, s[12:13]
	s_cbranch_vccz .LBB1_74
.LBB1_36:
	s_not_b64 s[16:17], s[52:53]
	s_andn2_b64 vcc, exec, s[52:53]
	s_cbranch_vccnz .LBB1_38

.LBB1_61:
	ds_read_b128 v[4:7], v226
	ds_read_b128 v[8:11], v226 offset:16
	ds_read_b128 v[82:85], v226 offset:32
	ds_read_b128 v[86:89], v226 offset:48
	ds_read_b128 v[12:15], v206 offset:32768
	ds_read_b128 v[244:247], v206 offset:33792
	s_waitcnt lgkmcnt(4)
	v_fma_mix_f32 v66, v190, s42, v4 op_sel:[0,0,0] op_sel_hi:[1,0,0]
	v_fma_mix_f32 v67, v190, s42, v5 op_sel:[1,0,0] op_sel_hi:[1,0,0]
	v_fma_mix_f32 v68, v191, s42, v6 op_sel:[0,0,0] op_sel_hi:[1,0,0]
	v_fma_mix_f32 v69, v191, s42, v7 op_sel:[1,0,0] op_sel_hi:[1,0,0]
	v_fma_mix_f32 v70, v192, s42, v8 op_sel:[0,0,0] op_sel_hi:[1,0,0]
	v_fma_mix_f32 v71, v192, s42, v9 op_sel:[1,0,0] op_sel_hi:[1,0,0]
	v_fma_mix_f32 v72, v193, s42, v10 op_sel:[0,0,0] op_sel_hi:[1,0,0]
	v_fma_mix_f32 v73, v193, s42, v11 op_sel:[1,0,0] op_sel_hi:[1,0,0]
	s_waitcnt lgkmcnt(2)
	v_fma_mix_f32 v74, v186, s42, v82 op_sel:[0,0,0] op_sel_hi:[1,0,0]
	v_fma_mix_f32 v75, v186, s42, v83 op_sel:[1,0,0] op_sel_hi:[1,0,0]
	v_fma_mix_f32 v76, v187, s42, v84 op_sel:[0,0,0] op_sel_hi:[1,0,0]
	v_fma_mix_f32 v77, v187, s42, v85 op_sel:[1,0,0] op_sel_hi:[1,0,0]
	v_fma_mix_f32 v78, v188, s42, v86 op_sel:[0,0,0] op_sel_hi:[1,0,0]
	v_fma_mix_f32 v79, v188, s42, v87 op_sel:[1,0,0] op_sel_hi:[1,0,0]
	v_fma_mix_f32 v80, v189, s42, v88 op_sel:[0,0,0] op_sel_hi:[1,0,0]
	v_fma_mix_f32 v81, v189, s42, v89 op_sel:[1,0,0] op_sel_hi:[1,0,0]
	s_nop 1
	s_nop 0
	s_waitcnt lgkmcnt(1)
	v_mfma_f32_32x32x16_f16 v[66:81], v[12:15], v[198:201], v[66:81]
	s_waitcnt lgkmcnt(0)
	v_mfma_f32_32x32x16_f16 v[66:81], v[244:247], v[202:205], v[66:81]
	s_not_b64 s[16:17], s[0:1]
	s_andn2_b64 vcc, exec, s[0:1]
	s_cbranch_vccnz .LBB1_8
.LBB1_62:
	ds_read_b128 v[4:7], v226 offset:128
	ds_read_b128 v[8:11], v226 offset:144
	ds_read_b128 v[82:85], v226 offset:160
	ds_read_b128 v[86:89], v226 offset:176
	ds_read_b128 v[12:15], v206 offset:34816
	ds_read_b128 v[244:247], v206 offset:35840
	s_waitcnt lgkmcnt(4)
	v_fma_mix_f32 v50, v182, s42, v4 op_sel:[0,0,0] op_sel_hi:[1,0,0]
	v_fma_mix_f32 v51, v182, s42, v5 op_sel:[1,0,0] op_sel_hi:[1,0,0]
	v_fma_mix_f32 v52, v183, s42, v6 op_sel:[0,0,0] op_sel_hi:[1,0,0]
	v_fma_mix_f32 v53, v183, s42, v7 op_sel:[1,0,0] op_sel_hi:[1,0,0]
	v_fma_mix_f32 v54, v184, s42, v8 op_sel:[0,0,0] op_sel_hi:[1,0,0]
	v_fma_mix_f32 v55, v184, s42, v9 op_sel:[1,0,0] op_sel_hi:[1,0,0]
	v_fma_mix_f32 v56, v185, s42, v10 op_sel:[0,0,0] op_sel_hi:[1,0,0]
	v_fma_mix_f32 v57, v185, s42, v11 op_sel:[1,0,0] op_sel_hi:[1,0,0]
	s_waitcnt lgkmcnt(2)
	v_fma_mix_f32 v58, v178, s42, v82 op_sel:[0,0,0] op_sel_hi:[1,0,0]
	v_fma_mix_f32 v59, v178, s42, v83 op_sel:[1,0,0] op_sel_hi:[1,0,0]
	v_fma_mix_f32 v60, v179, s42, v84 op_sel:[0,0,0] op_sel_hi:[1,0,0]
	v_fma_mix_f32 v61, v179, s42, v85 op_sel:[1,0,0] op_sel_hi:[1,0,0]
	v_fma_mix_f32 v62, v180, s42, v86 op_sel:[0,0,0] op_sel_hi:[1,0,0]
	v_fma_mix_f32 v63, v180, s42, v87 op_sel:[1,0,0] op_sel_hi:[1,0,0]
	v_fma_mix_f32 v64, v181, s42, v88 op_sel:[0,0,0] op_sel_hi:[1,0,0]
	v_fma_mix_f32 v65, v181, s42, v89 op_sel:[1,0,0] op_sel_hi:[1,0,0]
	s_nop 1
	s_nop 0
	s_waitcnt lgkmcnt(1)
	v_mfma_f32_32x32x16_f16 v[50:65], v[12:15], v[198:201], v[50:65]
	s_waitcnt lgkmcnt(0)
	v_mfma_f32_32x32x16_f16 v[50:65], v[244:247], v[202:205], v[50:65]
	s_not_b64 s[18:19], s[6:7]
	s_andn2_b64 vcc, exec, s[6:7]
	s_cbranch_vccnz .LBB1_9
.LBB1_63:
	ds_read_b128 v[4:7], v226 offset:256
	ds_read_b128 v[8:11], v226 offset:272
	ds_read_b128 v[82:85], v226 offset:288
	ds_read_b128 v[86:89], v226 offset:304
	ds_read_b128 v[12:15], v206 offset:36864
	ds_read_b128 v[244:247], v206 offset:37888
	s_waitcnt lgkmcnt(4)
	v_fma_mix_f32 v34, v170, s42, v4 op_sel:[0,0,0] op_sel_hi:[1,0,0]
	v_fma_mix_f32 v35, v170, s42, v5 op_sel:[1,0,0] op_sel_hi:[1,0,0]
	v_fma_mix_f32 v36, v171, s42, v6 op_sel:[0,0,0] op_sel_hi:[1,0,0]
	v_fma_mix_f32 v37, v171, s42, v7 op_sel:[1,0,0] op_sel_hi:[1,0,0]
	v_fma_mix_f32 v38, v172, s42, v8 op_sel:[0,0,0] op_sel_hi:[1,0,0]
	v_fma_mix_f32 v39, v172, s42, v9 op_sel:[1,0,0] op_sel_hi:[1,0,0]
	v_fma_mix_f32 v40, v173, s42, v10 op_sel:[0,0,0] op_sel_hi:[1,0,0]
	v_fma_mix_f32 v41, v173, s42, v11 op_sel:[1,0,0] op_sel_hi:[1,0,0]
	s_waitcnt lgkmcnt(2)
	v_fma_mix_f32 v42, v174, s42, v82 op_sel:[0,0,0] op_sel_hi:[1,0,0]
	v_fma_mix_f32 v43, v174, s42, v83 op_sel:[1,0,0] op_sel_hi:[1,0,0]
	v_fma_mix_f32 v44, v175, s42, v84 op_sel:[0,0,0] op_sel_hi:[1,0,0]
	v_fma_mix_f32 v45, v175, s42, v85 op_sel:[1,0,0] op_sel_hi:[1,0,0]
	v_fma_mix_f32 v46, v176, s42, v86 op_sel:[0,0,0] op_sel_hi:[1,0,0]
	v_fma_mix_f32 v47, v176, s42, v87 op_sel:[1,0,0] op_sel_hi:[1,0,0]
	v_fma_mix_f32 v48, v177, s42, v88 op_sel:[0,0,0] op_sel_hi:[1,0,0]
	v_fma_mix_f32 v49, v177, s42, v89 op_sel:[1,0,0] op_sel_hi:[1,0,0]
	s_nop 1
	s_nop 0
	s_waitcnt lgkmcnt(1)
	v_mfma_f32_32x32x16_f16 v[34:49], v[12:15], v[198:201], v[34:49]
	s_waitcnt lgkmcnt(0)
	v_mfma_f32_32x32x16_f16 v[34:49], v[244:247], v[202:205], v[34:49]
	s_not_b64 s[20:21], s[4:5]
	s_andn2_b64 vcc, exec, s[4:5]
	s_cbranch_vccz .LBB1_10
	s_branch .LBB1_11

.LBB1_71:
	s_waitcnt vmcnt(4)
	ds_read_b128 v[4:7], v226 offset:512
	ds_read_b128 v[8:11], v226 offset:528
	ds_read_b128 v[114:117], v226 offset:544
	ds_read_b128 v[118:121], v226 offset:560
	ds_read_b128 v[12:15], v206 offset:40960
	ds_read_b128 v[244:247], v206 offset:41984
	s_waitcnt lgkmcnt(4)
	v_fma_mix_f32 v66, v190, s42, v4 op_sel:[0,0,0] op_sel_hi:[1,0,0]
	v_fma_mix_f32 v67, v190, s42, v5 op_sel:[1,0,0] op_sel_hi:[1,0,0]
	v_fma_mix_f32 v68, v191, s42, v6 op_sel:[0,0,0] op_sel_hi:[1,0,0]
	v_fma_mix_f32 v69, v191, s42, v7 op_sel:[1,0,0] op_sel_hi:[1,0,0]
	v_fma_mix_f32 v70, v192, s42, v8 op_sel:[0,0,0] op_sel_hi:[1,0,0]
	v_fma_mix_f32 v71, v192, s42, v9 op_sel:[1,0,0] op_sel_hi:[1,0,0]
	v_fma_mix_f32 v72, v193, s42, v10 op_sel:[0,0,0] op_sel_hi:[1,0,0]
	v_fma_mix_f32 v73, v193, s42, v11 op_sel:[1,0,0] op_sel_hi:[1,0,0]
	s_waitcnt lgkmcnt(2)
	v_fma_mix_f32 v74, v186, s42, v114 op_sel:[0,0,0] op_sel_hi:[1,0,0]
	v_fma_mix_f32 v75, v186, s42, v115 op_sel:[1,0,0] op_sel_hi:[1,0,0]
	v_fma_mix_f32 v76, v187, s42, v116 op_sel:[0,0,0] op_sel_hi:[1,0,0]
	v_fma_mix_f32 v77, v187, s42, v117 op_sel:[1,0,0] op_sel_hi:[1,0,0]
	v_fma_mix_f32 v78, v188, s42, v118 op_sel:[0,0,0] op_sel_hi:[1,0,0]
	v_fma_mix_f32 v79, v188, s42, v119 op_sel:[1,0,0] op_sel_hi:[1,0,0]
	v_fma_mix_f32 v80, v189, s42, v120 op_sel:[0,0,0] op_sel_hi:[1,0,0]
	v_fma_mix_f32 v81, v189, s42, v121 op_sel:[1,0,0] op_sel_hi:[1,0,0]
	s_nop 1
	s_nop 0
	s_waitcnt lgkmcnt(1)
	v_mfma_f32_32x32x16_f16 v[66:81], v[12:15], v[198:201], v[66:81]
	s_waitcnt lgkmcnt(0)
	v_mfma_f32_32x32x16_f16 v[66:81], v[244:247], v[202:205], v[66:81]
	s_not_b64 s[20:21], s[8:9]
	s_andn2_b64 vcc, exec, s[8:9]
	s_cbranch_vccnz .LBB1_34
.LBB1_72:
	s_waitcnt vmcnt(4)
	ds_read_b128 v[4:7], v226 offset:640
	ds_read_b128 v[8:11], v226 offset:656
	ds_read_b128 v[114:117], v226 offset:672
	ds_read_b128 v[118:121], v226 offset:688
	ds_read_b128 v[12:15], v206 offset:43008
	ds_read_b128 v[244:247], v206 offset:44032
	s_waitcnt lgkmcnt(4)
	v_fma_mix_f32 v50, v182, s42, v4 op_sel:[0,0,0] op_sel_hi:[1,0,0]
	v_fma_mix_f32 v51, v182, s42, v5 op_sel:[1,0,0] op_sel_hi:[1,0,0]
	v_fma_mix_f32 v52, v183, s42, v6 op_sel:[0,0,0] op_sel_hi:[1,0,0]
	v_fma_mix_f32 v53, v183, s42, v7 op_sel:[1,0,0] op_sel_hi:[1,0,0]
	v_fma_mix_f32 v54, v184, s42, v8 op_sel:[0,0,0] op_sel_hi:[1,0,0]
	v_fma_mix_f32 v55, v184, s42, v9 op_sel:[1,0,0] op_sel_hi:[1,0,0]
	v_fma_mix_f32 v56, v185, s42, v10 op_sel:[0,0,0] op_sel_hi:[1,0,0]
	v_fma_mix_f32 v57, v185, s42, v11 op_sel:[1,0,0] op_sel_hi:[1,0,0]
	s_waitcnt lgkmcnt(2)
	v_fma_mix_f32 v58, v178, s42, v114 op_sel:[0,0,0] op_sel_hi:[1,0,0]
	v_fma_mix_f32 v59, v178, s42, v115 op_sel:[1,0,0] op_sel_hi:[1,0,0]
	v_fma_mix_f32 v60, v179, s42, v116 op_sel:[0,0,0] op_sel_hi:[1,0,0]
	v_fma_mix_f32 v61, v179, s42, v117 op_sel:[1,0,0] op_sel_hi:[1,0,0]
	v_fma_mix_f32 v62, v180, s42, v118 op_sel:[0,0,0] op_sel_hi:[1,0,0]
	v_fma_mix_f32 v63, v180, s42, v119 op_sel:[1,0,0] op_sel_hi:[1,0,0]
	v_fma_mix_f32 v64, v181, s42, v120 op_sel:[0,0,0] op_sel_hi:[1,0,0]
	v_fma_mix_f32 v65, v181, s42, v121 op_sel:[1,0,0] op_sel_hi:[1,0,0]
	s_nop 1
	s_nop 0
	s_waitcnt lgkmcnt(1)
	v_mfma_f32_32x32x16_f16 v[50:65], v[12:15], v[198:201], v[50:65]
	s_waitcnt lgkmcnt(0)
	v_mfma_f32_32x32x16_f16 v[50:65], v[244:247], v[202:205], v[50:65]
	s_not_b64 s[22:23], s[14:15]
	s_andn2_b64 vcc, exec, s[14:15]
	s_cbranch_vccnz .LBB1_35
.LBB1_73:
	s_waitcnt vmcnt(4)
	ds_read_b128 v[4:7], v226 offset:768
	ds_read_b128 v[8:11], v226 offset:784
	ds_read_b128 v[114:117], v226 offset:800
	ds_read_b128 v[118:121], v226 offset:816
	ds_read_b128 v[12:15], v206 offset:45056
	ds_read_b128 v[244:247], v206 offset:46080
	s_waitcnt lgkmcnt(4)
	v_fma_mix_f32 v34, v170, s42, v4 op_sel:[0,0,0] op_sel_hi:[1,0,0]
	v_fma_mix_f32 v35, v170, s42, v5 op_sel:[1,0,0] op_sel_hi:[1,0,0]
	v_fma_mix_f32 v36, v171, s42, v6 op_sel:[0,0,0] op_sel_hi:[1,0,0]
	v_fma_mix_f32 v37, v171, s42, v7 op_sel:[1,0,0] op_sel_hi:[1,0,0]
	v_fma_mix_f32 v38, v172, s42, v8 op_sel:[0,0,0] op_sel_hi:[1,0,0]
	v_fma_mix_f32 v39, v172, s42, v9 op_sel:[1,0,0] op_sel_hi:[1,0,0]
	v_fma_mix_f32 v40, v173, s42, v10 op_sel:[0,0,0] op_sel_hi:[1,0,0]
	v_fma_mix_f32 v41, v173, s42, v11 op_sel:[1,0,0] op_sel_hi:[1,0,0]
	s_waitcnt lgkmcnt(2)
	v_fma_mix_f32 v42, v174, s42, v114 op_sel:[0,0,0] op_sel_hi:[1,0,0]
	v_fma_mix_f32 v43, v174, s42, v115 op_sel:[1,0,0] op_sel_hi:[1,0,0]
	v_fma_mix_f32 v44, v175, s42, v116 op_sel:[0,0,0] op_sel_hi:[1,0,0]
	v_fma_mix_f32 v45, v175, s42, v117 op_sel:[1,0,0] op_sel_hi:[1,0,0]
	v_fma_mix_f32 v46, v176, s42, v118 op_sel:[0,0,0] op_sel_hi:[1,0,0]
	v_fma_mix_f32 v47, v176, s42, v119 op_sel:[1,0,0] op_sel_hi:[1,0,0]
	v_fma_mix_f32 v48, v177, s42, v120 op_sel:[0,0,0] op_sel_hi:[1,0,0]
	v_fma_mix_f32 v49, v177, s42, v121 op_sel:[1,0,0] op_sel_hi:[1,0,0]
	s_nop 1
	s_nop 0
	s_waitcnt lgkmcnt(1)
	v_mfma_f32_32x32x16_f16 v[34:49], v[12:15], v[198:201], v[34:49]
	s_waitcnt lgkmcnt(0)
	v_mfma_f32_32x32x16_f16 v[34:49], v[244:247], v[202:205], v[34:49]
	s_not_b64 s[24:25], s[12:13]
	s_andn2_b64 vcc, exec, s[12:13]
	s_cbranch_vccnz .LBB1_36
.LBB1_74:
	s_waitcnt vmcnt(4)
	ds_read_b128 v[4:7], v226 offset:896
	ds_read_b128 v[8:11], v226 offset:912
	ds_read_b128 v[114:117], v226 offset:928
	ds_read_b128 v[118:121], v226 offset:944
	ds_read_b128 v[12:15], v206 offset:47104
	ds_read_b128 v[244:247], v206 offset:48128
	s_waitcnt lgkmcnt(4)
	v_fma_mix_f32 v18, v162, s42, v4 op_sel:[0,0,0] op_sel_hi:[1,0,0]
	v_fma_mix_f32 v19, v162, s42, v5 op_sel:[1,0,0] op_sel_hi:[1,0,0]
	v_fma_mix_f32 v20, v163, s42, v6 op_sel:[0,0,0] op_sel_hi:[1,0,0]
	v_fma_mix_f32 v21, v163, s42, v7 op_sel:[1,0,0] op_sel_hi:[1,0,0]
	v_fma_mix_f32 v22, v164, s42, v8 op_sel:[0,0,0] op_sel_hi:[1,0,0]
	v_fma_mix_f32 v23, v164, s42, v9 op_sel:[1,0,0] op_sel_hi:[1,0,0]
	v_fma_mix_f32 v24, v165, s42, v10 op_sel:[0,0,0] op_sel_hi:[1,0,0]
	v_fma_mix_f32 v25, v165, s42, v11 op_sel:[1,0,0] op_sel_hi:[1,0,0]
	s_waitcnt lgkmcnt(2)
	v_fma_mix_f32 v26, v166, s42, v114 op_sel:[0,0,0] op_sel_hi:[1,0,0]
	v_fma_mix_f32 v27, v166, s42, v115 op_sel:[1,0,0] op_sel_hi:[1,0,0]
	v_fma_mix_f32 v28, v167, s42, v116 op_sel:[0,0,0] op_sel_hi:[1,0,0]
	v_fma_mix_f32 v29, v167, s42, v117 op_sel:[1,0,0] op_sel_hi:[1,0,0]
	v_fma_mix_f32 v30, v168, s42, v118 op_sel:[0,0,0] op_sel_hi:[1,0,0]
	v_fma_mix_f32 v31, v168, s42, v119 op_sel:[1,0,0] op_sel_hi:[1,0,0]
	v_fma_mix_f32 v32, v169, s42, v120 op_sel:[0,0,0] op_sel_hi:[1,0,0]
	v_fma_mix_f32 v33, v169, s42, v121 op_sel:[1,0,0] op_sel_hi:[1,0,0]
	s_nop 1
	s_nop 0
	s_waitcnt lgkmcnt(1)
	v_mfma_f32_32x32x16_f16 v[18:33], v[12:15], v[198:201], v[18:33]
	s_waitcnt lgkmcnt(0)
	v_mfma_f32_32x32x16_f16 v[18:33], v[244:247], v[202:205], v[18:33]
	s_not_b64 s[16:17], s[52:53]
	s_andn2_b64 vcc, exec, s[52:53]
	s_cbranch_vccz .LBB1_37
	s_branch .LBB1_38

.LBB1_82:
	v_mov_b64_e32 v[82:83], 0
	v_mov_b64_e32 v[84:85], 0
	v_mov_b64_e32 v[86:87], 0
	v_mov_b64_e32 v[88:89], 0
	v_mov_b64_e32 v[90:91], 0
	v_mov_b64_e32 v[92:93], 0
	v_mov_b64_e32 v[94:95], 0
	v_mov_b64_e32 v[96:97], 0
	v_mov_b64_e32 v[98:99], 0
	v_mov_b64_e32 v[100:101], 0
	v_mov_b64_e32 v[102:103], 0
	v_mov_b64_e32 v[104:105], 0
	v_mov_b64_e32 v[106:107], 0
	v_mov_b64_e32 v[108:109], 0
	v_mov_b64_e32 v[110:111], 0
	v_mov_b64_e32 v[112:113], 0
	v_sub_f32_e32 v1, v243, v236
	v_cmp_le_f32_e32 vcc, s56, v1
	s_cbranch_vccnz .LBB1_22
	s_branch .LBB1_23
